# P7 dispatch: the (up to three) 16-row groups of a wave processed with all assignment loads in flight (was load->wait->slot->store per group)
# baseline (speedup 1.0000x reference)
.Lgat_nozero:
	s_lshr_b32 s14, s46, 4
	s_mul_i32 s0, s86, s83
	s_add_i32 s37, s82, s0
	s_lshl_b32 s23, s83, 3
	s_cmp_ge_i32 s37, s14
	s_cbranch_scc1 .Lgat_done
	s_add_u32 s30, s6, 0x300000
	s_addc_u32 s31, s7, 0
	s_add_u32 s32, s6, 0x500000
	s_addc_u32 s33, s7, 0
	s_add_u32 s34, s6, 0x900000
	s_addc_u32 s35, s7, 0
	v_lshl_add_u32 v2, s37, 6, v213
	v_lshlrev_b32_e32 v3, 2, v2
	global_load_dword v4, v3, s[30:31]
	global_load_dword v5, v3, s[32:33]
	s_mov_b32 s1, 1
	s_add_i32 s0, s37, s23
	s_cmp_lt_i32 s0, s14
	s_cbranch_scc0 .Lgat_issued
	s_mov_b32 s1, 2
	v_lshl_add_u32 v10, s0, 6, v213
	v_lshlrev_b32_e32 v11, 2, v10
	global_load_dword v12, v11, s[30:31]
	global_load_dword v13, v11, s[32:33]
	s_add_i32 s0, s0, s23
	s_cmp_lt_i32 s0, s14
	s_cbranch_scc0 .Lgat_issued
	s_mov_b32 s1, 3
	v_lshl_add_u32 v14, s0, 6, v213
	v_lshlrev_b32_e32 v15, 2, v14
	global_load_dword v16, v15, s[30:31]
	global_load_dword v17, v15, s[32:33]
	s_add_i32 s0, s0, s23
.Lgat_issued:
	s_waitcnt vmcnt(0)
	v_lshrrev_b32_e32 v8, 2, v2
	v_lshlrev_b32_e32 v6, 2, v4
	v_add_u32_e32 v7, 0x200c0, v6
	v_add_u32_e32 v6, 0x20150, v6
	ds_read_b32 v7, v7
	ds_read_b32 v6, v6
	s_waitcnt lgkmcnt(0)
	v_add3_u32 v5, v7, v6, v5
	v_lshlrev_b32_e32 v9, 2, v5
	global_store_dword v3, v5, s[34:35]
	global_store_dword v9, v8, s[26:27]
	s_cmp_lt_u32 s1, 2
	s_cbranch_scc1 .Lgat_done
	v_lshrrev_b32_e32 v8, 2, v10
	v_lshlrev_b32_e32 v6, 2, v12
	v_add_u32_e32 v7, 0x200c0, v6
	v_add_u32_e32 v6, 0x20150, v6
	ds_read_b32 v7, v7
	ds_read_b32 v6, v6
	s_waitcnt lgkmcnt(0)
	v_add3_u32 v13, v7, v6, v13
	v_lshlrev_b32_e32 v9, 2, v13
	global_store_dword v11, v13, s[34:35]
	global_store_dword v9, v8, s[26:27]
	s_cmp_lt_u32 s1, 3
	s_cbranch_scc1 .Lgat_done
	v_lshrrev_b32_e32 v8, 2, v14
	v_lshlrev_b32_e32 v6, 2, v16
	v_add_u32_e32 v7, 0x200c0, v6
	v_add_u32_e32 v6, 0x20150, v6
	ds_read_b32 v7, v7
	ds_read_b32 v6, v6
	s_waitcnt lgkmcnt(0)
	v_add3_u32 v17, v7, v6, v17
	v_lshlrev_b32_e32 v9, 2, v17
	global_store_dword v15, v17, s[34:35]
	global_store_dword v9, v8, s[26:27]
	s_mov_b32 s37, s0
	s_cmp_lt_i32 s37, s14
	s_cbranch_scc0 .Lgat_done
